# GDN item head: 68 dead instructions per item removed (16 spill reloads and 11 address chains left over from the moved prefetch, 20 orphan s_nop)
# speedup vs baseline: 1.0049x; 1.0014x over previous
.LBB0_221:
	s_memrealtime s[0:1]
	s_waitcnt vmcnt(8)
	s_lshl_b32 s100, s76, 4
	s_lshl_b32 s2, s76, 6
	s_and_b32 s100, s100, 0xfffff000
	s_and_b32 s2, s2, 0xfc0
	v_mov_b32_e32 v215, v237
	v_mov_b32_e32 v216, v236
	s_or_b32 s100, s100, s2
	s_bfe_u32 s101, s76, 0x20006
	s_lshl_b32 s74, s101, 2
	v_lshlrev_b32_e32 v38, 1, v215
	s_not_b32 s101, s2
	s_cmp_le_i32 s31, s101
	v_mov_b32_e32 v27, v141
	v_mov_b32_e32 v28, v141
	v_mov_b32_e32 v29, v141
	s_cbranch_scc1 .LBB0_223
	v_mov_b32_e32 v27, v172
	v_mov_b32_e32 v28, v173
	v_mov_b32_e32 v29, v174
.LBB0_223:
	v_mov_b32_e32 v30, 0
	s_cmp_le_i32 s52, s101
	v_mov_b32_e32 v32, 0
	v_mov_b32_e32 v31, 0
	v_mov_b32_e32 v33, 0
	s_cbranch_scc1 .LBB0_225
	v_mov_b32_e32 v31, v175
	v_mov_b32_e32 v32, v176
	v_mov_b32_e32 v33, v177
.LBB0_225:
	s_cmp_le_i32 s53, s101
	v_mov_b32_e32 v35, 0
	v_mov_b32_e32 v36, 0
	s_cbranch_scc1 .LBB0_227
	v_mov_b32_e32 v35, v178
	v_mov_b32_e32 v30, v179
	v_mov_b32_e32 v36, v180
.LBB0_227:
	s_lshl_b64 s[100:101], s[100:101], 9
	s_waitcnt lgkmcnt(0)
	v_add_f32_e32 v24, v206, v220
	s_mov_b32 s0, 0x41a00000
	v_cmp_nlt_f32_e32 vcc, s0, v24
	s_and_saveexec_b64 s[0:1], vcc
	s_cbranch_execz .LBB0_229
	v_mul_f32_e32 v24, 0x3fb8aa3b, v24
	v_exp_f32_e32 v68, v24
	s_mov_b32 s2, 0x3f2aaaab
	v_add_f32_e32 v54, 1.0, v68
	v_frexp_mant_f32_e32 v58, v54
	v_cvt_f64_f32_e32 v[24:25], v54
	v_frexp_exp_i32_f64_e32 v24, v[24:25]
	v_cmp_gt_f32_e32 vcc, s2, v58
	v_add_f32_e32 v55, -1.0, v54
	v_sub_f32_e32 v59, v55, v54
	v_subbrev_co_u32_e32 v62, vcc, 0, v24, vcc
	v_sub_u32_e32 v24, 0, v62
	v_sub_f32_e32 v55, v68, v55
	v_add_f32_e32 v59, 1.0, v59
	v_ldexp_f32 v25, v54, v24
	v_add_f32_e32 v55, v55, v59
	v_add_f32_e32 v54, -1.0, v25
	v_add_f32_e32 v58, 1.0, v25
	v_ldexp_f32 v24, v55, v24
	v_add_f32_e32 v55, 1.0, v54
	v_add_f32_e32 v59, -1.0, v58
	v_sub_f32_e32 v55, v25, v55
	v_sub_f32_e32 v25, v25, v59
	v_add_f32_e32 v55, v24, v55
	v_add_f32_e32 v24, v24, v25
	v_add_f32_e32 v63, v58, v24
	v_rcp_f32_e32 v65, v63
	v_sub_f32_e32 v25, v63, v58
	v_sub_f32_e32 v64, v24, v25
	v_add_f32_e32 v25, v54, v55
	v_mul_f32_e32 v67, v25, v65
	v_sub_f32_e32 v24, v25, v54
	v_mul_f32_e32 v54, v63, v67
	v_fma_f32 v58, v67, v63, -v54
	v_fmac_f32_e32 v58, v67, v64
	v_sub_f32_e32 v66, v55, v24
	v_add_f32_e32 v24, v54, v58
	v_sub_f32_e32 v55, v25, v24
	v_pk_add_f32 v[60:61], v[24:25], v[54:55] neg_lo:[0,1] neg_hi:[0,1]
	v_mov_b32_e32 v59, v24
	v_pk_add_f32 v[24:25], v[60:61], v[58:59] neg_lo:[0,1] neg_hi:[0,1]
	s_mov_b32 s2, 0x3f317218
	v_add_f32_e32 v25, v66, v25
	v_add_f32_e32 v24, v24, v25
	v_add_f32_e32 v25, v55, v24
	v_mul_f32_e32 v66, v65, v25
	v_mul_f32_e32 v54, v63, v66
	v_fma_f32 v58, v66, v63, -v54
	v_fmac_f32_e32 v58, v66, v64
	v_sub_f32_e32 v55, v55, v25
	v_add_f32_e32 v63, v24, v55
	v_add_f32_e32 v24, v54, v58
	v_sub_f32_e32 v55, v25, v24
	v_pk_add_f32 v[60:61], v[24:25], v[54:55] neg_lo:[0,1] neg_hi:[0,1]
	v_mov_b32_e32 v59, v24
	v_pk_add_f32 v[24:25], v[60:61], v[58:59] neg_lo:[0,1] neg_hi:[0,1]
	s_nop 0
	v_add_f32_e32 v25, v63, v25
	v_add_f32_e32 v24, v24, v25
	v_add_f32_e32 v25, v67, v66
	v_add_f32_e32 v24, v55, v24
	v_sub_f32_e32 v54, v25, v67
	v_mul_f32_e32 v24, v65, v24
	v_sub_f32_e32 v54, v66, v54
	v_add_f32_e32 v54, v54, v24
	v_add_f32_e32 v58, v25, v54
	v_mul_f32_e32 v59, v58, v58
	v_fmamk_f32 v24, v59, 0x3e9b6dac, v208
	v_fmaak_f32 v143, v59, v24, 0x3f2aaada
	v_cvt_f32_i32_e32 v24, v62
	v_sub_f32_e32 v25, v58, v25
	v_sub_f32_e32 v25, v54, v25
	v_ldexp_f32 v60, v25, 1
	v_mul_f32_e32 v25, v58, v59
	v_ldexp_f32 v55, v58, 1
	v_pk_mul_f32 v[58:59], v[24:25], v[142:143]
	s_nop 0
	v_fma_f32 v54, v24, s2, -v58
	v_fmac_f32_e32 v54, 0xb102e308, v24
	v_pk_add_f32 v[24:25], v[58:59], v[54:55]
	s_mov_b32 s2, 0x7f800000
	v_sub_f32_e32 v55, v25, v55
	v_sub_f32_e32 v55, v59, v55
	v_add_f32_e32 v61, v60, v55
	v_mov_b32_e32 v60, v58
	v_pk_add_f32 v[58:59], v[24:25], v[58:59] neg_lo:[0,1] neg_hi:[0,1]
	v_pk_add_f32 v[62:63], v[24:25], v[60:61]
	v_mov_b32_e32 v55, v24
	v_mov_b32_e32 v59, v63
	v_pk_add_f32 v[64:65], v[54:55], v[58:59] neg_lo:[0,1] neg_hi:[0,1]
	v_pk_add_f32 v[54:55], v[54:55], v[58:59]
	v_mov_b32_e32 v60, v61
	v_pk_add_f32 v[58:59], v[54:55], v[24:25] op_sel:[1,0] op_sel_hi:[0,1] neg_lo:[0,1] neg_hi:[0,1]
	v_pk_add_f32 v[66:67], v[62:63], v[58:59] op_sel_hi:[1,0] neg_lo:[0,1] neg_hi:[0,1]
	v_mov_b32_e32 v62, v63
	v_mov_b32_e32 v63, v55
	v_pk_mov_b32 v[58:59], v[24:25], v[58:59] op_sel:[1,0]
	v_mov_b32_e32 v61, v24
	v_pk_add_f32 v[58:59], v[62:63], v[58:59] neg_lo:[0,1] neg_hi:[0,1]
	v_mov_b32_e32 v66, v64
	v_pk_add_f32 v[24:25], v[60:61], v[58:59] neg_lo:[0,1] neg_hi:[0,1]
	v_mov_b32_e32 v65, v55
	v_pk_add_f32 v[58:59], v[66:67], v[24:25]
	v_cmp_neq_f32_e32 vcc, s2, v68
	v_pk_add_f32 v[60:61], v[58:59], v[58:59] op_sel:[0,1] op_sel_hi:[1,0]
	s_mov_b32 s2, 0x33800000
	v_pk_add_f32 v[54:55], v[54:55], v[60:61] op_sel:[1,0] op_sel_hi:[0,1]
	v_mov_b32_e32 v59, v54
	v_pk_add_f32 v[62:63], v[58:59], v[64:65] neg_lo:[0,1] neg_hi:[0,1]
	v_mov_b32_e32 v25, v60
	v_sub_f32_e32 v55, v58, v62
	v_pk_add_f32 v[24:25], v[24:25], v[62:63] neg_lo:[0,1] neg_hi:[0,1]
	v_sub_f32_e32 v55, v64, v55
	v_add_f32_e32 v24, v24, v55
	v_add_f32_e32 v24, v24, v25
	v_add_f32_e32 v24, v54, v24
	v_cndmask_b32_e32 v24, v211, v24, vcc
	v_cmp_ngt_f32_e32 vcc, -1.0, v68
	s_nop 1
	v_cndmask_b32_e32 v24, v212, v24, vcc
	v_cmp_neq_f32_e32 vcc, -1.0, v68
	s_nop 1
	v_cndmask_b32_e32 v24, v213, v24, vcc
	v_cmp_lt_f32_e64 vcc, |v68|, s2
	s_nop 1
	v_cndmask_b32_e32 v24, v24, v68, vcc
